# v042 + peer_u loop: the 8 expert-offset LDS reads of each half issued together (hipcc had 6 of them serialized, each with lgkmcnt(0) before its two gathers)
# baseline (speedup 1.0000x reference)
; __device__ __forceinline__ int dot16_i8(const u32x4 a, const u32x4 x) {
;     int d = __builtin_amdgcn_sdot4((int)a.x, (int)x.x, 0, false); d = __builtin_amdgcn_sdot4((int)a.y, (int)x.y, d, false);
;     d = __builtin_amdgcn_sdot4((int)a.z, (int)x.z, d, false); return __builtin_amdgcn_sdot4((int)a.w, (int)x.w, d, false);
; }
; __device__ __forceinline__ int row16_tsum(const int (&d)[16], int i) {
;     int e0, e1, e2, e3, e4, e5, e6, e7, f0, f1, f2, f3;
;     asm volatile("s_nop 1\n\t"
;         "v_add_u32_dpp %0, %8, %8 row_mirror row_mask:0xf bank_mask:0xf\n\t"   "v_add_u32_dpp %1, %9, %9 row_mirror row_mask:0xf bank_mask:0xf\n\t"
;         "v_add_u32_dpp %2, %10, %10 row_mirror row_mask:0xf bank_mask:0xf\n\t" "v_add_u32_dpp %3, %11, %11 row_mirror row_mask:0xf bank_mask:0xf\n\t"
;         "v_add_u32_dpp %4, %12, %12 row_mirror row_mask:0xf bank_mask:0xf\n\t" "v_add_u32_dpp %5, %13, %13 row_mirror row_mask:0xf bank_mask:0xf\n\t"
;         "v_add_u32_dpp %6, %14, %14 row_mirror row_mask:0xf bank_mask:0xf\n\t" "v_add_u32_dpp %7, %15, %15 row_mirror row_mask:0xf bank_mask:0xf\n\t"
;         "v_add_u32_dpp %0, %16, %16 row_mirror row_mask:0xf bank_mask:0xc\n\t" "v_add_u32_dpp %1, %17, %17 row_mirror row_mask:0xf bank_mask:0xc\n\t"
;         "v_add_u32_dpp %2, %18, %18 row_mirror row_mask:0xf bank_mask:0xc\n\t" "v_add_u32_dpp %3, %19, %19 row_mirror row_mask:0xf bank_mask:0xc\n\t"
;         "v_add_u32_dpp %4, %20, %20 row_mirror row_mask:0xf bank_mask:0xc\n\t" "v_add_u32_dpp %5, %21, %21 row_mirror row_mask:0xf bank_mask:0xc\n\t"
;         "v_add_u32_dpp %6, %22, %22 row_mirror row_mask:0xf bank_mask:0xc\n\t" "v_add_u32_dpp %7, %23, %23 row_mirror row_mask:0xf bank_mask:0xc\n\t"
;         "s_nop 1"
;         : "=&v"(e0), "=&v"(e1), "=&v"(e2), "=&v"(e3), "=&v"(e4), "=&v"(e5), "=&v"(e6), "=&v"(e7)
;         : "v"(d[0]), "v"(d[1]), "v"(d[2]), "v"(d[3]), "v"(d[4]), "v"(d[5]), "v"(d[6]), "v"(d[7]), "v"(d[8]), "v"(d[9]), "v"(d[10]), "v"(d[11]), "v"(d[12]), "v"(d[13]), "v"(d[14]), "v"(d[15]));
;     asm volatile(
;         "v_add_u32_dpp %0, %4, %4 row_half_mirror row_mask:0xf bank_mask:0xf\n\t" "v_add_u32_dpp %1, %5, %5 row_half_mirror row_mask:0xf bank_mask:0xf\n\t"
;         "v_add_u32_dpp %2, %6, %6 row_half_mirror row_mask:0xf bank_mask:0xf\n\t" "v_add_u32_dpp %3, %7, %7 row_half_mirror row_mask:0xf bank_mask:0xf\n\t"
.LBB0_829:
	v_mov_b32_e32 v57, 0
	s_waitcnt vmcnt(28)
	v_dot4c_i32_i8_e32 v57, v66, v86
	v_mov_b32_e32 v66, 0
	s_waitcnt vmcnt(27)
	v_dot4c_i32_i8_e32 v66, v62, v86
	v_mov_b32_e32 v62, 0
	s_waitcnt vmcnt(26)
	v_dot4c_i32_i8_e32 v62, v58, v86
	v_mov_b32_e32 v58, 0
	s_waitcnt vmcnt(25)
	v_dot4c_i32_i8_e32 v58, v50, v86
	v_mov_b32_e32 v50, 0
	s_waitcnt vmcnt(24)
	v_dot4c_i32_i8_e32 v50, v46, v86
	v_mov_b32_e32 v46, 0
	s_waitcnt vmcnt(23)
	v_dot4c_i32_i8_e32 v46, v42, v86
	v_mov_b32_e32 v42, 0
	s_waitcnt vmcnt(22)
	v_dot4c_i32_i8_e32 v42, v38, v86
	v_mov_b32_e32 v38, 0
	s_add_i32 s5, s7, 3
	s_waitcnt vmcnt(21)
	v_dot4c_i32_i8_e32 v38, v34, v86
	v_mov_b32_e32 v34, 0
	s_min_i32 s5, s5, s1
	s_waitcnt vmcnt(20)
	v_dot4c_i32_i8_e32 v34, v30, v86
	v_mov_b32_e32 v30, 0
	s_mul_i32 s5, s5, s54
	s_waitcnt vmcnt(19)
	v_dot4c_i32_i8_e32 v30, v26, v86
	v_mov_b32_e32 v26, 0
	s_add_i32 s8, s5, s0
	v_lshlrev_b32_e32 v6, 8, v170
	v_lshlrev_b32_e32 v7, 8, v151
	s_waitcnt vmcnt(18)
	v_dot4c_i32_i8_e32 v26, v22, v86
	v_mov_b32_e32 v22, 0
	v_and_b32_e32 v6, 0x3fff00, v6
	v_and_b32_e32 v7, 0x3fff00, v7
	s_ashr_i32 s9, s8, 31
	v_mov_b32_e32 v54, 0
	v_mov_b32_e32 v55, 0
	v_mov_b32_e32 v56, 0
	s_waitcnt vmcnt(17)
	v_dot4c_i32_i8_e32 v22, v18, v86
	v_mov_b32_e32 v18, 0
	ds_write2st64_b32 v1, v6, v7 offset0:2 offset1:3
	s_lshl_b64 s[10:11], s[8:9], 9
	v_dot4c_i32_i8_e32 v54, v78, v86
	v_dot4c_i32_i8_e32 v55, v74, v86
	v_dot4c_i32_i8_e32 v56, v70, v86
	s_waitcnt vmcnt(16)
	v_dot4c_i32_i8_e32 v18, v14, v86
	v_lshl_add_u64 v[6:7], v[160:161], 0, s[10:11]
	s_lshl_b64 s[8:9], s[8:9], 8
	v_dot4c_i32_i8_e32 v54, v79, v87
	v_dot4c_i32_i8_e32 v55, v75, v87
	v_dot4c_i32_i8_e32 v56, v71, v87
	v_dot4c_i32_i8_e32 v57, v67, v87
	v_dot4c_i32_i8_e32 v66, v63, v87
	v_dot4c_i32_i8_e32 v62, v59, v87
	v_dot4c_i32_i8_e32 v58, v51, v87
	v_dot4c_i32_i8_e32 v50, v47, v87
	v_dot4c_i32_i8_e32 v46, v43, v87
	v_dot4c_i32_i8_e32 v42, v39, v87
	v_dot4c_i32_i8_e32 v38, v35, v87
	v_dot4c_i32_i8_e32 v34, v31, v87
	v_dot4c_i32_i8_e32 v30, v27, v87
	v_dot4c_i32_i8_e32 v26, v23, v87
	v_dot4c_i32_i8_e32 v22, v19, v87
	v_dot4c_i32_i8_e32 v18, v15, v87
	global_load_dword v170, v[6:7], off
	global_load_dword v151, v[6:7], off offset:256
	v_lshl_add_u64 v[6:7], v[164:165], 0, s[8:9]
	v_dot4c_i32_i8_e32 v54, v80, v88
	v_dot4c_i32_i8_e32 v55, v76, v88
	v_dot4c_i32_i8_e32 v56, v72, v88
	v_dot4c_i32_i8_e32 v57, v68, v88
	v_dot4c_i32_i8_e32 v66, v64, v88
	v_dot4c_i32_i8_e32 v62, v60, v88
	v_dot4c_i32_i8_e32 v58, v52, v88
	v_dot4c_i32_i8_e32 v50, v48, v88
	v_dot4c_i32_i8_e32 v46, v44, v88
	v_dot4c_i32_i8_e32 v42, v40, v88
	v_dot4c_i32_i8_e32 v38, v36, v88
	v_dot4c_i32_i8_e32 v34, v32, v88
	v_dot4c_i32_i8_e32 v30, v28, v88
	v_dot4c_i32_i8_e32 v26, v24, v88
	v_dot4c_i32_i8_e32 v22, v20, v88
	v_dot4c_i32_i8_e32 v18, v16, v88
	global_load_dwordx4 v[6:9], v[6:7], off
	v_dot4c_i32_i8_e32 v54, v81, v89
	v_dot4c_i32_i8_e32 v55, v77, v89
	v_dot4c_i32_i8_e32 v56, v73, v89
	v_dot4c_i32_i8_e32 v57, v69, v89
	v_dot4c_i32_i8_e32 v66, v65, v89
	v_dot4c_i32_i8_e32 v62, v61, v89
	v_dot4c_i32_i8_e32 v58, v53, v89
	v_dot4c_i32_i8_e32 v50, v49, v89
	v_dot4c_i32_i8_e32 v46, v45, v89
	v_dot4c_i32_i8_e32 v42, v41, v89
	v_dot4c_i32_i8_e32 v38, v37, v89
	v_dot4c_i32_i8_e32 v34, v33, v89
	v_dot4c_i32_i8_e32 v30, v29, v89
	v_dot4c_i32_i8_e32 v26, v25, v89
	v_dot4c_i32_i8_e32 v22, v21, v89
	v_dot4c_i32_i8_e32 v18, v17, v89
	s_nop 1
	v_add_u32_dpp v14, v54, v54 row_mirror row_mask:0xf bank_mask:0xf
	v_add_u32_dpp v15, v55, v55 row_mirror row_mask:0xf bank_mask:0xf
	v_add_u32_dpp v16, v56, v56 row_mirror row_mask:0xf bank_mask:0xf
	v_add_u32_dpp v17, v57, v57 row_mirror row_mask:0xf bank_mask:0xf
	v_add_u32_dpp v19, v66, v66 row_mirror row_mask:0xf bank_mask:0xf
	v_add_u32_dpp v20, v62, v62 row_mirror row_mask:0xf bank_mask:0xf
	v_add_u32_dpp v21, v58, v58 row_mirror row_mask:0xf bank_mask:0xf
	v_add_u32_dpp v23, v50, v50 row_mirror row_mask:0xf bank_mask:0xf
	v_add_u32_dpp v14, v46, v46 row_mirror row_mask:0xf bank_mask:0xc
	v_add_u32_dpp v15, v42, v42 row_mirror row_mask:0xf bank_mask:0xc
	v_add_u32_dpp v16, v38, v38 row_mirror row_mask:0xf bank_mask:0xc
	v_add_u32_dpp v17, v34, v34 row_mirror row_mask:0xf bank_mask:0xc
	v_add_u32_dpp v19, v30, v30 row_mirror row_mask:0xf bank_mask:0xc
	v_add_u32_dpp v20, v26, v26 row_mirror row_mask:0xf bank_mask:0xc
	v_add_u32_dpp v21, v22, v22 row_mirror row_mask:0xf bank_mask:0xc
	v_add_u32_dpp v23, v18, v18 row_mirror row_mask:0xf bank_mask:0xc
	s_nop 1
	v_mov_b32_e32 v57, 0
	v_add_u32_dpp v18, v14, v14 row_half_mirror row_mask:0xf bank_mask:0xf
	v_add_u32_dpp v22, v15, v15 row_half_mirror row_mask:0xf bank_mask:0xf
	v_add_u32_dpp v24, v16, v16 row_half_mirror row_mask:0xf bank_mask:0xf
	v_add_u32_dpp v25, v17, v17 row_half_mirror row_mask:0xf bank_mask:0xf
	v_add_u32_dpp v18, v19, v19 row_half_mirror row_mask:0xf bank_mask:0xa
	v_add_u32_dpp v22, v20, v20 row_half_mirror row_mask:0xf bank_mask:0xa
	v_add_u32_dpp v24, v21, v21 row_half_mirror row_mask:0xf bank_mask:0xa
	v_add_u32_dpp v25, v23, v23 row_half_mirror row_mask:0xf bank_mask:0xa
	s_nop 1
	s_waitcnt vmcnt(16)
	v_dot4c_i32_i8_e32 v57, v138, v86
	v_mov_b32_e32 v138, 0
	v_add_u32_dpp v14, v18, v18 quad_perm:[3,2,1,0] row_mask:0xf bank_mask:0xf bound_ctrl:1
	v_add_u32_dpp v15, v24, v24 quad_perm:[3,2,1,0] row_mask:0xf bank_mask:0xf bound_ctrl:1
	v_add_u32_dpp v16, v22, v22 quad_perm:[3,2,1,0] row_mask:0xf bank_mask:0xf bound_ctrl:1
	v_add_u32_dpp v17, v25, v25 quad_perm:[3,2,1,0] row_mask:0xf bank_mask:0xf bound_ctrl:1
	v_cndmask_b32_e64 v14, v15, v14, s[2:3]
	v_cndmask_b32_e64 v15, v17, v16, s[2:3]
	s_waitcnt vmcnt(15)
	v_dot4c_i32_i8_e32 v138, v130, v86
	v_add_u32_dpp v14, v14, v14 quad_perm:[1,0,3,2] row_mask:0xf bank_mask:0xf bound_ctrl:1
	v_add_u32_dpp v15, v15, v15 quad_perm:[1,0,3,2] row_mask:0xf bank_mask:0xf bound_ctrl:1
	v_cndmask_b32_e64 v54, v15, v14, s[38:39]
	ds_read2_b32 v[14:15], v168 offset0:128 offset1:132
	ds_read2_b32 v[16:17], v168 offset0:136 offset1:140
	ds_read2_b32 v[204:205], v168 offset0:144 offset1:148
	ds_read2_b32 v[206:207], v168 offset0:152 offset1:156
	ds_read2_b32 v[208:209], v168 offset0:160 offset1:164
	ds_read2_b32 v[210:211], v168 offset0:168 offset1:172
	ds_read2_b32 v[212:213], v168 offset0:176 offset1:180
	ds_read2_b32 v[214:215], v168 offset0:184 offset1:188
	v_dot4c_i32_i8_e32 v138, v131, v87
	v_mov_b32_e32 v131, 0
	s_waitcnt vmcnt(13)
	v_dot4c_i32_i8_e32 v131, v126, v86
	s_waitcnt lgkmcnt(0)
	v_add_u32_e32 v14, v14, v150
	global_load_dwordx4 v[78:81], v14, s[52:53]
	v_add_u32_e32 v14, v15, v150
	global_load_dwordx4 v[74:77], v14, s[52:53]
	s_waitcnt lgkmcnt(0)
	v_add_u32_e32 v14, v16, v150
	global_load_dwordx4 v[70:73], v14, s[52:53]
	v_add_u32_e32 v14, v17, v150
	global_load_dwordx4 v[66:69], v14, s[52:53]
	v_mov_b32_e32 v126, 0
	s_waitcnt vmcnt(16)
	v_dot4c_i32_i8_e32 v126, v122, v86
	v_mov_b32_e32 v122, 0
	s_waitcnt vmcnt(15)
	v_dot4c_i32_i8_e32 v122, v114, v86
	v_add_u32_e32 v14, v204, v150
	global_load_dwordx4 v[62:65], v14, s[52:53]
	v_add_u32_e32 v14, v205, v150
	global_load_dwordx4 v[58:61], v14, s[52:53]
	v_mov_b32_e32 v114, 0
	s_waitcnt vmcnt(16)
	v_dot4c_i32_i8_e32 v114, v110, v86
	v_mov_b32_e32 v110, 0
	s_waitcnt vmcnt(15)
	v_dot4c_i32_i8_e32 v110, v106, v86
	v_add_u32_e32 v14, v206, v150
	global_load_dwordx4 v[50:53], v14, s[52:53]
	v_add_u32_e32 v14, v207, v150
	global_load_dwordx4 v[46:49], v14, s[52:53]
	v_mov_b32_e32 v106, 0
	s_waitcnt vmcnt(16)
	v_dot4c_i32_i8_e32 v106, v98, v86
	v_mov_b32_e32 v98, 0
	s_waitcnt vmcnt(15)
	v_dot4c_i32_i8_e32 v98, v94, v86
	v_add_u32_e32 v14, v208, v150
	global_load_dwordx4 v[42:45], v14, s[52:53]
	v_add_u32_e32 v14, v209, v150
	global_load_dwordx4 v[38:41], v14, s[52:53]
	v_mov_b32_e32 v94, 0
	s_waitcnt vmcnt(16)
	v_dot4c_i32_i8_e32 v94, v90, v86
	v_mov_b32_e32 v90, 0
	v_mov_b32_e32 v55, 0
	v_add_u32_e32 v14, v210, v150
	global_load_dwordx4 v[34:37], v14, s[52:53]
	v_add_u32_e32 v14, v211, v150
	global_load_dwordx4 v[30:33], v14, s[52:53]
	v_mov_b32_e32 v56, 0
	s_waitcnt vmcnt(17)
	v_dot4c_i32_i8_e32 v90, v82, v86
	v_mov_b32_e32 v82, 0
	v_dot4c_i32_i8_e32 v55, v146, v86
	v_add_u32_e32 v14, v212, v150
	global_load_dwordx4 v[26:29], v14, s[52:53]
	v_add_u32_e32 v14, v213, v150
	global_load_dwordx4 v[22:25], v14, s[52:53]
	v_dot4c_i32_i8_e32 v56, v142, v86
	v_mov_b32_e32 v130, 0
	v_dot4c_i32_i8_e32 v90, v83, v87
	s_waitcnt vmcnt(18)
	v_dot4c_i32_i8_e32 v82, v102, v86
	v_mov_b32_e32 v83, 0
	v_dot4c_i32_i8_e32 v55, v147, v87
	v_dot4c_i32_i8_e32 v56, v143, v87
	v_dot4c_i32_i8_e32 v57, v139, v87
	v_dot4c_i32_i8_e32 v130, v134, v86
	v_dot4c_i32_i8_e32 v82, v103, v87
	s_waitcnt vmcnt(17)
	v_dot4c_i32_i8_e32 v83, v118, v86
	v_add_u32_e32 v14, v214, v150
	v_dot4c_i32_i8_e32 v55, v148, v88
	v_dot4c_i32_i8_e32 v56, v144, v88
	v_dot4c_i32_i8_e32 v57, v140, v88
	v_dot4c_i32_i8_e32 v130, v135, v87
	v_dot4c_i32_i8_e32 v131, v127, v87
	v_dot4c_i32_i8_e32 v126, v123, v87
	v_dot4c_i32_i8_e32 v122, v115, v87
	v_dot4c_i32_i8_e32 v114, v111, v87
	v_dot4c_i32_i8_e32 v110, v107, v87
	v_dot4c_i32_i8_e32 v106, v99, v87
	v_dot4c_i32_i8_e32 v98, v95, v87
	v_dot4c_i32_i8_e32 v94, v91, v87
	v_dot4c_i32_i8_e32 v82, v104, v88
	v_dot4c_i32_i8_e32 v83, v119, v87
	global_load_dwordx4 v[18:21], v14, s[52:53]
	v_add_u32_e32 v14, v215, v150
	v_dot4c_i32_i8_e32 v55, v149, v89
	v_dot4c_i32_i8_e32 v56, v145, v89
	v_dot4c_i32_i8_e32 v57, v141, v89
	v_dot4c_i32_i8_e32 v138, v132, v88
	v_dot4c_i32_i8_e32 v130, v136, v88
	v_dot4c_i32_i8_e32 v131, v128, v88
	v_dot4c_i32_i8_e32 v126, v124, v88
	v_dot4c_i32_i8_e32 v122, v116, v88
	v_dot4c_i32_i8_e32 v114, v112, v88
	v_dot4c_i32_i8_e32 v110, v108, v88
	v_dot4c_i32_i8_e32 v106, v100, v88
	v_dot4c_i32_i8_e32 v98, v96, v88
	v_dot4c_i32_i8_e32 v94, v92, v88
	v_dot4c_i32_i8_e32 v90, v84, v88
	v_dot4c_i32_i8_e32 v82, v105, v89
	v_dot4c_i32_i8_e32 v83, v120, v88
	global_load_dwordx4 v[14:17], v14, s[52:53]
	v_dot4c_i32_i8_e32 v138, v133, v89
	v_dot4c_i32_i8_e32 v130, v137, v89
	v_dot4c_i32_i8_e32 v131, v129, v89
	v_dot4c_i32_i8_e32 v126, v125, v89
	v_dot4c_i32_i8_e32 v122, v117, v89
	v_dot4c_i32_i8_e32 v114, v113, v89
	v_dot4c_i32_i8_e32 v110, v109, v89
	v_dot4c_i32_i8_e32 v106, v101, v89
	v_dot4c_i32_i8_e32 v98, v97, v89
	v_dot4c_i32_i8_e32 v94, v93, v89
	v_dot4c_i32_i8_e32 v90, v85, v89
	v_dot4c_i32_i8_e32 v83, v121, v89
	s_nop 1
	v_add_u32_dpp v84, v55, v55 row_mirror row_mask:0xf bank_mask:0xf
	v_add_u32_dpp v85, v56, v56 row_mirror row_mask:0xf bank_mask:0xf
	v_add_u32_dpp v86, v57, v57 row_mirror row_mask:0xf bank_mask:0xf
	v_add_u32_dpp v87, v138, v138 row_mirror row_mask:0xf bank_mask:0xf
	v_add_u32_dpp v88, v130, v130 row_mirror row_mask:0xf bank_mask:0xf
	v_add_u32_dpp v89, v131, v131 row_mirror row_mask:0xf bank_mask:0xf
	v_add_u32_dpp v91, v126, v126 row_mirror row_mask:0xf bank_mask:0xf
	v_add_u32_dpp v92, v122, v122 row_mirror row_mask:0xf bank_mask:0xf
	v_add_u32_dpp v84, v114, v114 row_mirror row_mask:0xf bank_mask:0xc
	v_add_u32_dpp v85, v110, v110 row_mirror row_mask:0xf bank_mask:0xc
	v_add_u32_dpp v86, v106, v106 row_mirror row_mask:0xf bank_mask:0xc
	v_add_u32_dpp v87, v98, v98 row_mirror row_mask:0xf bank_mask:0xc
	v_add_u32_dpp v88, v94, v94 row_mirror row_mask:0xf bank_mask:0xc
	v_add_u32_dpp v89, v90, v90 row_mirror row_mask:0xf bank_mask:0xc
	v_add_u32_dpp v91, v82, v82 row_mirror row_mask:0xf bank_mask:0xc
	v_add_u32_dpp v92, v83, v83 row_mirror row_mask:0xf bank_mask:0xc
	s_nop 1
	v_mov_b32_e32 v146, 0
	v_add_u32_dpp v55, v84, v84 row_half_mirror row_mask:0xf bank_mask:0xf
	v_add_u32_dpp v56, v85, v85 row_half_mirror row_mask:0xf bank_mask:0xf
	v_add_u32_dpp v57, v86, v86 row_half_mirror row_mask:0xf bank_mask:0xf
	v_add_u32_dpp v82, v87, v87 row_half_mirror row_mask:0xf bank_mask:0xf
	v_add_u32_dpp v55, v88, v88 row_half_mirror row_mask:0xf bank_mask:0xa
	v_add_u32_dpp v56, v89, v89 row_half_mirror row_mask:0xf bank_mask:0xa
	v_add_u32_dpp v57, v91, v91 row_half_mirror row_mask:0xf bank_mask:0xa
	v_add_u32_dpp v82, v92, v92 row_half_mirror row_mask:0xf bank_mask:0xa
	s_nop 1
	s_waitcnt vmcnt(15)
	v_dot4c_i32_i8_e32 v146, v78, v10
	v_mov_b32_e32 v78, 0
	v_add_u32_dpp v55, v55, v55 quad_perm:[3,2,1,0] row_mask:0xf bank_mask:0xf bound_ctrl:1
	v_add_u32_dpp v57, v57, v57 quad_perm:[3,2,1,0] row_mask:0xf bank_mask:0xf bound_ctrl:1
	v_add_u32_dpp v56, v56, v56 quad_perm:[3,2,1,0] row_mask:0xf bank_mask:0xf bound_ctrl:1
	v_add_u32_dpp v82, v82, v82 quad_perm:[3,2,1,0] row_mask:0xf bank_mask:0xf bound_ctrl:1
	v_cndmask_b32_e64 v55, v57, v55, s[2:3]
	v_cndmask_b32_e64 v56, v82, v56, s[2:3]
	s_waitcnt vmcnt(14)
	v_dot4c_i32_i8_e32 v78, v74, v10
	v_add_u32_dpp v55, v55, v55 quad_perm:[1,0,3,2] row_mask:0xf bank_mask:0xf bound_ctrl:1
	v_add_u32_dpp v56, v56, v56 quad_perm:[1,0,3,2] row_mask:0xf bank_mask:0xf bound_ctrl:1
	v_cndmask_b32_e64 v55, v56, v55, s[38:39]
	ds_read2_b32 v[56:57], v168 offset0:192 offset1:196
	ds_read2_b32 v[82:83], v168 offset0:200 offset1:204
	ds_read2_b32 v[204:205], v168 offset0:208 offset1:212
	ds_read2_b32 v[206:207], v168 offset0:216 offset1:220
	ds_read2_b32 v[208:209], v168 offset0:224 offset1:228
	ds_read2_b32 v[210:211], v168 offset0:232 offset1:236
	ds_read2_b32 v[212:213], v168 offset0:240 offset1:244
	ds_read2_b32 v[214:215], v168 offset0:248 offset1:252
	v_mov_b32_e32 v74, 0
	s_waitcnt vmcnt(13)
	v_dot4c_i32_i8_e32 v74, v70, v10
	v_mov_b32_e32 v70, 0
	s_waitcnt lgkmcnt(0)
	v_add_u32_e32 v56, v56, v150
	global_load_dwordx4 v[142:145], v56, s[52:53]
	v_add_u32_e32 v56, v57, v150
	global_load_dwordx4 v[138:141], v56, s[52:53]
	s_waitcnt lgkmcnt(0)
	v_add_u32_e32 v56, v82, v150
	global_load_dwordx4 v[134:137], v56, s[52:53]
	v_add_u32_e32 v56, v83, v150
	global_load_dwordx4 v[130:133], v56, s[52:53]
	s_waitcnt vmcnt(16)
	v_dot4c_i32_i8_e32 v70, v66, v10
	v_mov_b32_e32 v66, 0
	s_waitcnt vmcnt(15)
	v_dot4c_i32_i8_e32 v66, v62, v10
	v_mov_b32_e32 v62, 0
	v_add_u32_e32 v56, v204, v150
	global_load_dwordx4 v[126:129], v56, s[52:53]
	v_add_u32_e32 v56, v205, v150
	global_load_dwordx4 v[122:125], v56, s[52:53]
	s_waitcnt vmcnt(16)
	v_dot4c_i32_i8_e32 v62, v58, v10
	v_mov_b32_e32 v58, 0
	s_waitcnt vmcnt(15)
	v_dot4c_i32_i8_e32 v58, v50, v10
	v_mov_b32_e32 v50, 0
	v_add_u32_e32 v56, v206, v150
	global_load_dwordx4 v[118:121], v56, s[52:53]
	v_add_u32_e32 v56, v207, v150
	global_load_dwordx4 v[114:117], v56, s[52:53]
	s_waitcnt vmcnt(16)
	v_dot4c_i32_i8_e32 v50, v46, v10
	v_mov_b32_e32 v46, 0
	s_ashr_i32 s5, s4, 31
	s_waitcnt vmcnt(15)
	v_dot4c_i32_i8_e32 v46, v42, v10
	v_add_u32_e32 v56, v208, v150
	global_load_dwordx4 v[110:113], v56, s[52:53]
	v_add_u32_e32 v56, v209, v150
	global_load_dwordx4 v[106:109], v56, s[52:53]
	v_mov_b32_e32 v42, 0
	s_lshl_b64 s[8:9], s[4:5], 12
	s_waitcnt vmcnt(16)
	v_dot4c_i32_i8_e32 v42, v38, v10
	v_mov_b32_e32 v38, 0
	v_add_u32_e32 v56, v210, v150
	global_load_dwordx4 v[102:105], v56, s[52:53]
	v_add_u32_e32 v56, v211, v150
	global_load_dwordx4 v[98:101], v56, s[52:53]
	s_waitcnt vmcnt(17)
	v_dot4c_i32_i8_e32 v38, v34, v10
	v_mov_b32_e32 v34, 0
	s_waitcnt vmcnt(16)
	v_dot4c_i32_i8_e32 v34, v30, v10
	v_mov_b32_e32 v30, 0
	v_add_u32_e32 v56, v212, v150
	global_load_dwordx4 v[94:97], v56, s[52:53]
	v_add_u32_e32 v56, v213, v150
	global_load_dwordx4 v[90:93], v56, s[52:53]
	s_waitcnt vmcnt(17)
	v_dot4c_i32_i8_e32 v30, v26, v10
	v_mov_b32_e32 v26, 0
	s_waitcnt vmcnt(16)
	v_dot4c_i32_i8_e32 v26, v22, v10
	v_mov_b32_e32 v22, 0
	v_add_u32_e32 v56, v214, v150
	global_load_dwordx4 v[86:89], v56, s[52:53]
	v_add_u32_e32 v56, v215, v150
	global_load_dwordx4 v[82:85], v56, s[52:53]
	v_lshl_add_u64 v[56:57], v[166:167], 0, s[8:9]
	s_add_i32 s8, s7, 4
	s_min_i32 s8, s8, s1
	s_mul_i32 s8, s8, s54
	global_store_dword v[56:57], v54, off
	global_store_dword v[56:57], v55, off offset:256
	s_add_i32 s8, s8, s0
	v_lshlrev_b32_e32 v54, 8, v171
	v_lshlrev_b32_e32 v55, 8, v169
	s_add_i32 s10, s7, 1
	v_and_b32_e32 v54, 0x3fff00, v54
	v_and_b32_e32 v55, 0x3fff00, v55
	s_ashr_i32 s9, s8, 31
	s_waitcnt vmcnt(19)
	v_dot4c_i32_i8_e32 v22, v18, v10
	v_mov_b32_e32 v18, 0
	s_waitcnt vmcnt(37)
	s_min_i32 s5, s10, s1
	ds_write2st64_b32 v1, v54, v55 offset1:1
	s_lshl_b64 s[10:11], s[8:9], 9
	s_waitcnt vmcnt(18)
	v_dot4c_i32_i8_e32 v18, v14, v10
	v_lshl_add_u64 v[54:55], v[160:161], 0, s[10:11]
	s_lshl_b64 s[8:9], s[8:9], 8
	v_dot4c_i32_i8_e32 v146, v79, v11
	v_dot4c_i32_i8_e32 v78, v75, v11
	v_dot4c_i32_i8_e32 v74, v71, v11
	v_dot4c_i32_i8_e32 v70, v67, v11
	v_dot4c_i32_i8_e32 v66, v63, v11
	v_dot4c_i32_i8_e32 v62, v59, v11
	v_dot4c_i32_i8_e32 v58, v51, v11
	v_dot4c_i32_i8_e32 v50, v47, v11
	v_dot4c_i32_i8_e32 v46, v43, v11
	v_dot4c_i32_i8_e32 v42, v39, v11
	v_dot4c_i32_i8_e32 v38, v35, v11
	v_dot4c_i32_i8_e32 v34, v31, v11
	v_dot4c_i32_i8_e32 v30, v27, v11
	v_dot4c_i32_i8_e32 v26, v23, v11
	v_dot4c_i32_i8_e32 v22, v19, v11
	v_dot4c_i32_i8_e32 v18, v15, v11
	global_load_dword v171, v[54:55], off
	global_load_dword v169, v[54:55], off offset:256
	v_lshl_add_u64 v[54:55], v[164:165], 0, s[8:9]
	v_dot4c_i32_i8_e32 v146, v80, v12
	v_dot4c_i32_i8_e32 v78, v76, v12
	v_dot4c_i32_i8_e32 v74, v72, v12
	v_dot4c_i32_i8_e32 v70, v68, v12
	v_dot4c_i32_i8_e32 v66, v64, v12
	v_dot4c_i32_i8_e32 v62, v60, v12
	v_dot4c_i32_i8_e32 v58, v52, v12
	v_dot4c_i32_i8_e32 v50, v48, v12
	v_dot4c_i32_i8_e32 v46, v44, v12
	v_dot4c_i32_i8_e32 v42, v40, v12
	v_dot4c_i32_i8_e32 v38, v36, v12
	v_dot4c_i32_i8_e32 v34, v32, v12
	v_dot4c_i32_i8_e32 v30, v28, v12
	v_dot4c_i32_i8_e32 v26, v24, v12
	v_dot4c_i32_i8_e32 v22, v20, v12
	v_dot4c_i32_i8_e32 v18, v16, v12
	global_load_dwordx4 v[54:57], v[54:55], off
	v_dot4c_i32_i8_e32 v146, v81, v13
	v_dot4c_i32_i8_e32 v78, v77, v13
	v_dot4c_i32_i8_e32 v74, v73, v13
	v_dot4c_i32_i8_e32 v70, v69, v13
	v_dot4c_i32_i8_e32 v66, v65, v13
	v_dot4c_i32_i8_e32 v62, v61, v13
	v_dot4c_i32_i8_e32 v58, v53, v13
	v_dot4c_i32_i8_e32 v50, v49, v13
	v_dot4c_i32_i8_e32 v46, v45, v13
	v_dot4c_i32_i8_e32 v42, v41, v13
	v_dot4c_i32_i8_e32 v38, v37, v13
	v_dot4c_i32_i8_e32 v34, v33, v13
	v_dot4c_i32_i8_e32 v30, v29, v13
	v_dot4c_i32_i8_e32 v26, v25, v13
	v_dot4c_i32_i8_e32 v22, v21, v13
	v_dot4c_i32_i8_e32 v18, v17, v13
	s_nop 1
	v_add_u32_dpp v14, v146, v146 row_mirror row_mask:0xf bank_mask:0xf
	v_add_u32_dpp v15, v78, v78 row_mirror row_mask:0xf bank_mask:0xf
	v_add_u32_dpp v16, v74, v74 row_mirror row_mask:0xf bank_mask:0xf
	v_add_u32_dpp v17, v70, v70 row_mirror row_mask:0xf bank_mask:0xf
	v_add_u32_dpp v19, v66, v66 row_mirror row_mask:0xf bank_mask:0xf
	v_add_u32_dpp v20, v62, v62 row_mirror row_mask:0xf bank_mask:0xf
	v_add_u32_dpp v21, v58, v58 row_mirror row_mask:0xf bank_mask:0xf
	v_add_u32_dpp v23, v50, v50 row_mirror row_mask:0xf bank_mask:0xf
	v_add_u32_dpp v14, v46, v46 row_mirror row_mask:0xf bank_mask:0xc
	v_add_u32_dpp v15, v42, v42 row_mirror row_mask:0xf bank_mask:0xc
	v_add_u32_dpp v16, v38, v38 row_mirror row_mask:0xf bank_mask:0xc
	v_add_u32_dpp v17, v34, v34 row_mirror row_mask:0xf bank_mask:0xc
	v_add_u32_dpp v19, v30, v30 row_mirror row_mask:0xf bank_mask:0xc
	v_add_u32_dpp v20, v26, v26 row_mirror row_mask:0xf bank_mask:0xc
	v_add_u32_dpp v21, v22, v22 row_mirror row_mask:0xf bank_mask:0xc
	v_add_u32_dpp v23, v18, v18 row_mirror row_mask:0xf bank_mask:0xc
	s_nop 1
	v_mov_b32_e32 v146, 0
	v_add_u32_dpp v18, v14, v14 row_half_mirror row_mask:0xf bank_mask:0xf
	v_add_u32_dpp v22, v15, v15 row_half_mirror row_mask:0xf bank_mask:0xf
	v_add_u32_dpp v24, v16, v16 row_half_mirror row_mask:0xf bank_mask:0xf
	v_add_u32_dpp v25, v17, v17 row_half_mirror row_mask:0xf bank_mask:0xf
	v_add_u32_dpp v18, v19, v19 row_half_mirror row_mask:0xf bank_mask:0xa
	v_add_u32_dpp v22, v20, v20 row_half_mirror row_mask:0xf bank_mask:0xa
	v_add_u32_dpp v24, v21, v21 row_half_mirror row_mask:0xf bank_mask:0xa
	v_add_u32_dpp v25, v23, v23 row_half_mirror row_mask:0xf bank_mask:0xa
	s_nop 1
	s_waitcnt vmcnt(20)
	v_dot4c_i32_i8_e32 v146, v142, v10
	v_mov_b32_e32 v142, 0
	v_add_u32_dpp v14, v18, v18 quad_perm:[3,2,1,0] row_mask:0xf bank_mask:0xf bound_ctrl:1
	v_add_u32_dpp v15, v24, v24 quad_perm:[3,2,1,0] row_mask:0xf bank_mask:0xf bound_ctrl:1
	v_add_u32_dpp v16, v22, v22 quad_perm:[3,2,1,0] row_mask:0xf bank_mask:0xf bound_ctrl:1
	v_add_u32_dpp v17, v25, v25 quad_perm:[3,2,1,0] row_mask:0xf bank_mask:0xf bound_ctrl:1
	v_cndmask_b32_e64 v14, v15, v14, s[2:3]
	v_cndmask_b32_e64 v15, v17, v16, s[2:3]
	s_waitcnt vmcnt(19)
	v_dot4c_i32_i8_e32 v142, v138, v10
	v_add_u32_dpp v14, v14, v14 quad_perm:[1,0,3,2] row_mask:0xf bank_mask:0xf bound_ctrl:1
	v_add_u32_dpp v15, v15, v15 quad_perm:[1,0,3,2] row_mask:0xf bank_mask:0xf bound_ctrl:1
	v_cndmask_b32_e64 v172, v15, v14, s[38:39]
	ds_read2_b32 v[14:15], v168 offset1:4
	ds_read2_b32 v[16:17], v168 offset0:8 offset1:12
	ds_read2_b32 v[204:205], v168 offset0:16 offset1:20
	ds_read2_b32 v[206:207], v168 offset0:24 offset1:28
	ds_read2_b32 v[208:209], v168 offset0:32 offset1:36
	ds_read2_b32 v[210:211], v168 offset0:40 offset1:44
	ds_read2_b32 v[212:213], v168 offset0:48 offset1:52
	ds_read2_b32 v[214:215], v168 offset0:56 offset1:60
	v_mov_b32_e32 v138, 0
	s_waitcnt vmcnt(18)
	v_dot4c_i32_i8_e32 v138, v134, v10
	v_mov_b32_e32 v134, 0
	s_waitcnt lgkmcnt(0)
	v_add_u32_e32 v14, v14, v150
	global_load_dwordx4 v[78:81], v14, s[52:53]
	v_add_u32_e32 v14, v15, v150
	global_load_dwordx4 v[74:77], v14, s[52:53]
	s_waitcnt lgkmcnt(0)
	v_add_u32_e32 v14, v16, v150
	global_load_dwordx4 v[70:73], v14, s[52:53]
	v_add_u32_e32 v14, v17, v150
	global_load_dwordx4 v[66:69], v14, s[52:53]
	s_waitcnt vmcnt(21)
	v_dot4c_i32_i8_e32 v134, v130, v10
	v_mov_b32_e32 v130, 0
	s_waitcnt vmcnt(20)
	v_dot4c_i32_i8_e32 v130, v126, v10
	v_mov_b32_e32 v126, 0
	v_add_u32_e32 v14, v204, v150
	global_load_dwordx4 v[62:65], v14, s[52:53]
	v_add_u32_e32 v14, v205, v150
	global_load_dwordx4 v[58:61], v14, s[52:53]
	s_waitcnt vmcnt(21)
	v_dot4c_i32_i8_e32 v126, v122, v10
	v_mov_b32_e32 v122, 0
	s_waitcnt vmcnt(20)
	v_dot4c_i32_i8_e32 v122, v118, v10
	v_mov_b32_e32 v118, 0
	v_add_u32_e32 v14, v206, v150
	global_load_dwordx4 v[50:53], v14, s[52:53]
	v_add_u32_e32 v14, v207, v150
	global_load_dwordx4 v[46:49], v14, s[52:53]
	s_waitcnt vmcnt(21)
	v_dot4c_i32_i8_e32 v118, v114, v10
	v_mov_b32_e32 v114, 0
	s_waitcnt vmcnt(20)
	v_dot4c_i32_i8_e32 v114, v110, v10
	v_mov_b32_e32 v110, 0
	v_add_u32_e32 v14, v208, v150
	global_load_dwordx4 v[42:45], v14, s[52:53]
	v_add_u32_e32 v14, v209, v150
	global_load_dwordx4 v[38:41], v14, s[52:53]
	s_waitcnt vmcnt(21)
	v_dot4c_i32_i8_e32 v110, v106, v10
	v_mov_b32_e32 v106, 0
	s_waitcnt vmcnt(20)
	v_dot4c_i32_i8_e32 v106, v102, v10
	v_mov_b32_e32 v102, 0
	v_add_u32_e32 v14, v210, v150
	global_load_dwordx4 v[34:37], v14, s[52:53]
	v_add_u32_e32 v14, v211, v150
	global_load_dwordx4 v[30:33], v14, s[52:53]
	s_waitcnt vmcnt(21)
	v_dot4c_i32_i8_e32 v102, v98, v10
	v_mov_b32_e32 v98, 0
	s_waitcnt vmcnt(20)
	v_dot4c_i32_i8_e32 v98, v94, v10
	v_mov_b32_e32 v94, 0
	v_add_u32_e32 v14, v212, v150
	global_load_dwordx4 v[26:29], v14, s[52:53]
	v_add_u32_e32 v14, v213, v150
	global_load_dwordx4 v[22:25], v14, s[52:53]
	s_waitcnt vmcnt(21)
	v_dot4c_i32_i8_e32 v94, v90, v10
	v_mov_b32_e32 v90, 0
	s_waitcnt vmcnt(20)
	v_dot4c_i32_i8_e32 v90, v86, v10
	v_mov_b32_e32 v86, 0
	s_waitcnt vmcnt(19)
;     ...
;         for (int n = 0; n < NT; n += 2) {
;             PU_BODY(n, ma0, mb0, x0);
;             PU_BODY(n + 1, ma1, mb1, x1);
;         }
	v_dot4c_i32_i8_e32 v86, v82, v10
	v_add_u32_e32 v14, v214, v150
	v_dot4c_i32_i8_e32 v146, v143, v11
	v_dot4c_i32_i8_e32 v142, v139, v11
	v_dot4c_i32_i8_e32 v138, v135, v11
	v_dot4c_i32_i8_e32 v134, v131, v11
	v_dot4c_i32_i8_e32 v130, v127, v11
	v_dot4c_i32_i8_e32 v126, v123, v11
	v_dot4c_i32_i8_e32 v122, v119, v11
	v_dot4c_i32_i8_e32 v118, v115, v11
	v_dot4c_i32_i8_e32 v114, v111, v11
	v_dot4c_i32_i8_e32 v110, v107, v11
	v_dot4c_i32_i8_e32 v106, v103, v11
	v_dot4c_i32_i8_e32 v102, v99, v11
	v_dot4c_i32_i8_e32 v98, v95, v11
	v_dot4c_i32_i8_e32 v94, v91, v11
	v_dot4c_i32_i8_e32 v90, v87, v11
	v_dot4c_i32_i8_e32 v86, v83, v11
	global_load_dwordx4 v[18:21], v14, s[52:53]
	v_add_u32_e32 v14, v215, v150
	v_dot4c_i32_i8_e32 v146, v144, v12
	v_dot4c_i32_i8_e32 v142, v140, v12
	v_dot4c_i32_i8_e32 v138, v136, v12
	v_dot4c_i32_i8_e32 v134, v132, v12
	v_dot4c_i32_i8_e32 v130, v128, v12
	v_dot4c_i32_i8_e32 v126, v124, v12
	v_dot4c_i32_i8_e32 v122, v120, v12
	v_dot4c_i32_i8_e32 v118, v116, v12
	v_dot4c_i32_i8_e32 v114, v112, v12
	v_dot4c_i32_i8_e32 v110, v108, v12
	v_dot4c_i32_i8_e32 v106, v104, v12
	v_dot4c_i32_i8_e32 v102, v100, v12
	v_dot4c_i32_i8_e32 v98, v96, v12
	v_dot4c_i32_i8_e32 v94, v92, v12
	v_dot4c_i32_i8_e32 v90, v88, v12
	v_dot4c_i32_i8_e32 v86, v84, v12
	global_load_dwordx4 v[14:17], v14, s[52:53]
	v_dot4c_i32_i8_e32 v146, v145, v13
	v_dot4c_i32_i8_e32 v142, v141, v13
	v_dot4c_i32_i8_e32 v138, v137, v13
	v_dot4c_i32_i8_e32 v134, v133, v13
	v_dot4c_i32_i8_e32 v130, v129, v13
	v_dot4c_i32_i8_e32 v126, v125, v13
	v_dot4c_i32_i8_e32 v122, v121, v13
	v_dot4c_i32_i8_e32 v118, v117, v13
	v_dot4c_i32_i8_e32 v114, v113, v13
	v_dot4c_i32_i8_e32 v110, v109, v13
	v_dot4c_i32_i8_e32 v106, v105, v13
	v_dot4c_i32_i8_e32 v102, v101, v13
	v_dot4c_i32_i8_e32 v98, v97, v13
	v_dot4c_i32_i8_e32 v94, v93, v13
	v_dot4c_i32_i8_e32 v90, v89, v13
	v_dot4c_i32_i8_e32 v86, v85, v13
	s_nop 1
	v_add_u32_dpp v10, v146, v146 row_mirror row_mask:0xf bank_mask:0xf
	v_add_u32_dpp v11, v142, v142 row_mirror row_mask:0xf bank_mask:0xf
	v_add_u32_dpp v12, v138, v138 row_mirror row_mask:0xf bank_mask:0xf
	v_add_u32_dpp v13, v134, v134 row_mirror row_mask:0xf bank_mask:0xf
	v_add_u32_dpp v82, v130, v130 row_mirror row_mask:0xf bank_mask:0xf
	v_add_u32_dpp v83, v126, v126 row_mirror row_mask:0xf bank_mask:0xf
	v_add_u32_dpp v84, v122, v122 row_mirror row_mask:0xf bank_mask:0xf
	v_add_u32_dpp v85, v118, v118 row_mirror row_mask:0xf bank_mask:0xf
	v_add_u32_dpp v10, v114, v114 row_mirror row_mask:0xf bank_mask:0xc
	v_add_u32_dpp v11, v110, v110 row_mirror row_mask:0xf bank_mask:0xc
	v_add_u32_dpp v12, v106, v106 row_mirror row_mask:0xf bank_mask:0xc
	v_add_u32_dpp v13, v102, v102 row_mirror row_mask:0xf bank_mask:0xc
	v_add_u32_dpp v82, v98, v98 row_mirror row_mask:0xf bank_mask:0xc
	v_add_u32_dpp v83, v94, v94 row_mirror row_mask:0xf bank_mask:0xc
	v_add_u32_dpp v84, v90, v90 row_mirror row_mask:0xf bank_mask:0xc
	v_add_u32_dpp v85, v86, v86 row_mirror row_mask:0xf bank_mask:0xc
	s_nop 1
	s_mul_i32 s5, s5, s54
	v_add_u32_dpp v86, v10, v10 row_half_mirror row_mask:0xf bank_mask:0xf
	v_add_u32_dpp v87, v11, v11 row_half_mirror row_mask:0xf bank_mask:0xf
	v_add_u32_dpp v88, v12, v12 row_half_mirror row_mask:0xf bank_mask:0xf
	v_add_u32_dpp v89, v13, v13 row_half_mirror row_mask:0xf bank_mask:0xf
	v_add_u32_dpp v86, v82, v82 row_half_mirror row_mask:0xf bank_mask:0xa
	v_add_u32_dpp v87, v83, v83 row_half_mirror row_mask:0xf bank_mask:0xa
	v_add_u32_dpp v88, v84, v84 row_half_mirror row_mask:0xf bank_mask:0xa
	v_add_u32_dpp v89, v85, v85 row_half_mirror row_mask:0xf bank_mask:0xa
	s_nop 1
	s_add_i32 s8, s5, s0
	s_ashr_i32 s9, s8, 31
	v_add_u32_dpp v10, v86, v86 quad_perm:[3,2,1,0] row_mask:0xf bank_mask:0xf bound_ctrl:1
	v_add_u32_dpp v11, v88, v88 quad_perm:[3,2,1,0] row_mask:0xf bank_mask:0xf bound_ctrl:1
	v_add_u32_dpp v12, v87, v87 quad_perm:[3,2,1,0] row_mask:0xf bank_mask:0xf bound_ctrl:1
	v_add_u32_dpp v13, v89, v89 quad_perm:[3,2,1,0] row_mask:0xf bank_mask:0xf bound_ctrl:1
	v_cndmask_b32_e64 v10, v11, v10, s[2:3]
	v_cndmask_b32_e64 v11, v13, v12, s[2:3]
	s_lshl_b64 s[8:9], s[8:9], 12
	v_add_u32_dpp v10, v10, v10 quad_perm:[1,0,3,2] row_mask:0xf bank_mask:0xf bound_ctrl:1
	v_add_u32_dpp v11, v11, v11 quad_perm:[1,0,3,2] row_mask:0xf bank_mask:0xf bound_ctrl:1
	v_cndmask_b32_e64 v86, v11, v10, s[38:39]
	ds_read2_b32 v[10:11], v168 offset0:64 offset1:68
	ds_read2_b32 v[12:13], v168 offset0:72 offset1:76
	ds_read2_b32 v[204:205], v168 offset0:80 offset1:84
	ds_read2_b32 v[206:207], v168 offset0:88 offset1:92
	ds_read2_b32 v[208:209], v168 offset0:96 offset1:100
	ds_read2_b32 v[210:211], v168 offset0:104 offset1:108
	ds_read2_b32 v[212:213], v168 offset0:112 offset1:116
	ds_read2_b32 v[214:215], v168 offset0:120 offset1:124
	s_add_i32 s7, s7, 2
	s_add_i32 s4, s4, s55
	s_cmp_ge_i32 s7, s6
	s_waitcnt lgkmcnt(0)
	v_add_u32_e32 v10, v10, v150
	global_load_dwordx4 v[146:149], v10, s[52:53]
	v_add_u32_e32 v10, v11, v150
	global_load_dwordx4 v[142:145], v10, s[52:53]
	s_waitcnt lgkmcnt(0)
	v_add_u32_e32 v10, v12, v150
	global_load_dwordx4 v[138:141], v10, s[52:53]
	v_add_u32_e32 v10, v13, v150
	global_load_dwordx4 v[130:133], v10, s[52:53]
	v_add_u32_e32 v10, v204, v150
	global_load_dwordx4 v[134:137], v10, s[52:53]
	v_add_u32_e32 v10, v205, v150
	global_load_dwordx4 v[126:129], v10, s[52:53]
	v_add_u32_e32 v10, v206, v150
	global_load_dwordx4 v[122:125], v10, s[52:53]
	v_add_u32_e32 v10, v207, v150
	global_load_dwordx4 v[114:117], v10, s[52:53]
	v_add_u32_e32 v10, v208, v150
	global_load_dwordx4 v[110:113], v10, s[52:53]
	v_add_u32_e32 v10, v209, v150
	global_load_dwordx4 v[106:109], v10, s[52:53]
	v_add_u32_e32 v10, v210, v150
	global_load_dwordx4 v[98:101], v10, s[52:53]
	v_add_u32_e32 v10, v211, v150
	global_load_dwordx4 v[94:97], v10, s[52:53]
	v_add_u32_e32 v10, v212, v150
	global_load_dwordx4 v[90:93], v10, s[52:53]
	v_add_u32_e32 v10, v213, v150
	global_load_dwordx4 v[82:85], v10, s[52:53]
	v_add_u32_e32 v10, v214, v150
	global_load_dwordx4 v[102:105], v10, s[52:53]
	v_add_u32_e32 v10, v215, v150
	global_load_dwordx4 v[118:121], v10, s[52:53]
	v_lshl_add_u64 v[10:11], v[166:167], 0, s[8:9]
	global_store_dword v[10:11], v172, off
	global_store_dword v[10:11], v86, off offset:256
	v_mov_b64_e32 v[88:89], v[4:5]
	v_mov_b64_e32 v[86:87], v[2:3]
	v_mov_b64_e32 v[12:13], v[8:9]
	s_waitcnt vmcnt(34)
	v_mov_b64_e32 v[2:3], v[54:55]
	v_mov_b64_e32 v[10:11], v[6:7]
	v_mov_b64_e32 v[4:5], v[56:57]
	s_waitcnt vmcnt(37)
	s_cbranch_scc0 .LBB0_829
	s_branch .LBB0_826
